# baseline (speedup 1.0000x reference)
.Levt_join2:
	s_nop 1
	v_mul_f32_e32 v54, s26, v54
	v_mul_f32_e32 v55, s26, v55
	v_mul_f32_e32 v56, s26, v56
	v_mul_f32_e32 v57, s26, v57
	v_mul_f32_e32 v58, s26, v58
	v_mul_f32_e32 v59, s26, v59
	v_mul_f32_e32 v60, s26, v60
	v_mul_f32_e32 v61, s26, v61
	v_mul_f32_e32 v62, s26, v62
	v_mul_f32_e32 v63, s26, v63
	v_mul_f32_e32 v64, s26, v64
	v_mul_f32_e32 v65, s26, v65
	v_mul_f32_e32 v66, s26, v66
	v_mul_f32_e32 v67, s26, v67
	v_mul_f32_e32 v68, s26, v68
	v_mul_f32_e32 v69, s26, v69
	v_max3_f32 v70, v54, v55, v56
	v_max3_f32 v71, v57, v58, v59
	v_max3_f32 v72, v60, v61, v62
	v_max3_f32 v73, v63, v64, v65
	v_max3_f32 v74, v66, v67, v68
	v_max3_f32 v70, v70, v71, v72
	v_max3_f32 v73, v73, v74, v69
	v_max_f32_e32 v70, v70, v73
	v_mov_b32_e32 v71, v70
	s_nop 1
	v_permlane32_swap_b32_e32 v70, v71
	v_max_f32_e32 v70, v70, v71
	ds_write_b32 v173, v70 offset:512
	s_waitcnt lgkmcnt(0)
	s_barrier
	ds_read_b32 v71, v75
	s_waitcnt lgkmcnt(0)
	v_max_f32_e32 v70, v70, v71
	v_sub_f32_e32 v54, v54, v70
	v_sub_f32_e32 v55, v55, v70
	v_sub_f32_e32 v56, v56, v70
	v_sub_f32_e32 v57, v57, v70
	v_sub_f32_e32 v58, v58, v70
	v_sub_f32_e32 v59, v59, v70
	v_sub_f32_e32 v60, v60, v70
	v_sub_f32_e32 v61, v61, v70
	v_sub_f32_e32 v62, v62, v70
	v_sub_f32_e32 v63, v63, v70
	v_sub_f32_e32 v64, v64, v70
	v_sub_f32_e32 v65, v65, v70
	v_sub_f32_e32 v66, v66, v70
	v_sub_f32_e32 v67, v67, v70
	v_sub_f32_e32 v68, v68, v70
	v_sub_f32_e32 v69, v69, v70
	v_exp_f32_e32 v54, v54
	v_exp_f32_e32 v55, v55
	v_exp_f32_e32 v56, v56
	v_exp_f32_e32 v57, v57
	s_nop 0
	ds_write_b128 v76, v[54:57]
	v_exp_f32_e32 v58, v58
	v_exp_f32_e32 v59, v59
	v_exp_f32_e32 v60, v60
	v_exp_f32_e32 v61, v61
	s_nop 0
	ds_write_b128 v76, v[58:61] offset:1024
	v_exp_f32_e32 v62, v62
	v_exp_f32_e32 v63, v63
	v_exp_f32_e32 v64, v64
	v_exp_f32_e32 v65, v65
	s_nop 0
	ds_write_b128 v76, v[62:65] offset:2048
	v_exp_f32_e32 v66, v66
	v_exp_f32_e32 v67, v67
	v_exp_f32_e32 v68, v68
	v_exp_f32_e32 v69, v69
	s_nop 0
	ds_write_b128 v76, v[66:69] offset:3072
	s_nop 0
	s_load_dwordx4 s[8:11], s[0:1], 0x48
	v_mov_b32_e32 v2, v174
	v_add_u32_e32 v10, v172, v2
	s_waitcnt vmcnt(1) lgkmcnt(0)
	s_barrier
	ds_read_b128 v[18:21], v10 offset:256
	ds_read_b128 v[22:25], v10 offset:288
	ds_read_b128 v[82:85], v10 offset:320
	ds_read_b128 v[86:89], v10 offset:352
	ds_read_b128 v[74:77], v10 offset:384
	ds_read_b128 v[78:81], v10 offset:416
	ds_read_b128 v[2:5], v213 offset:32768
	ds_read_b128 v[6:9], v213 offset:0
	ds_read_b128 v[66:69], v10 offset:448
	ds_read_b128 v[70:73], v10 offset:480
	ds_read_b128 v[10:13], v213 offset:1024
	s_waitcnt lgkmcnt(3)
	v_pk_mul_f32 v[26:27], v[8:9], v[20:21]
	v_pk_mul_f32 v[28:29], v[6:7], v[18:19]
	ds_read_b128 v[14:17], v213 offset:8192
	s_waitcnt lgkmcnt(1)
	v_pk_mul_f32 v[12:13], v[12:13], v[24:25]
	v_pk_mul_f32 v[10:11], v[10:11], v[22:23]
	v_pk_fma_f32 v[30:31], v[8:9], v[20:21], v[12:13]
	v_pk_fma_f32 v[32:33], v[6:7], v[18:19], v[10:11]
	v_cvt_pk_bf16_f32 v9, v12, v13
	v_cvt_pk_bf16_f32 v7, v26, v27
	v_cvt_pk_bf16_f32 v8, v10, v11
	v_cvt_pk_bf16_f32 v6, v28, v29
	ds_read_b128 v[10:13], v213 offset:33792
	s_nop 0
	v_mfma_f32_32x32x16_bf16 v[34:49], v[2:5], v[6:9], 0
	ds_read_b128 v[6:9], v213 offset:9216
	s_waitcnt lgkmcnt(2)
	v_mul_f32_e32 v26, v16, v20
	v_mul_f32_e32 v27, v17, v21
	v_pk_mul_f32 v[50:51], v[14:15], v[18:19]
	s_mov_b32 s4, 0x3727c5ac
	s_waitcnt lgkmcnt(0)
	v_pk_mul_f32 v[8:9], v[8:9], v[24:25]
	v_pk_mul_f32 v[28:29], v[6:7], v[22:23]
	v_pk_fma_f32 v[90:91], v[16:17], v[20:21], v[8:9]
	v_pk_fma_f32 v[92:93], v[14:15], v[18:19], v[28:29]
	ds_read_b128 v[14:17], v213 offset:2048
	v_cvt_pk_bf16_f32 v9, v8, v9
	v_cvt_pk_bf16_f32 v7, v26, v27
	v_cvt_pk_bf16_f32 v8, v28, v29
	ds_read_b128 v[26:29], v213 offset:3072
	v_cvt_pk_bf16_f32 v6, v50, v51
	s_waitcnt lgkmcnt(1)
	v_pk_mul_f32 v[94:95], v[14:15], v[82:83]
	s_mov_b32 s0, 0x3c800000
	v_mfma_f32_32x32x16_bf16 v[50:65], v[2:5], v[6:9], 0
	v_mul_f32_e32 v2, v16, v84
	v_mul_f32_e32 v3, v17, v85
	s_waitcnt lgkmcnt(0)
	v_mul_f32_e32 v4, v28, v88
	v_mul_f32_e32 v5, v29, v89
	v_pk_mul_f32 v[6:7], v[26:27], v[86:87]
	v_pk_fma_f32 v[8:9], v[16:17], v[84:85], v[4:5]
	v_cvt_pk_bf16_f32 v3, v2, v3
	v_pk_fma_f32 v[14:15], v[14:15], v[82:83], v[6:7]
	v_pk_add_f32 v[26:27], v[8:9], v[30:31]
	v_cvt_pk_bf16_f32 v5, v4, v5
	v_cvt_pk_bf16_f32 v4, v6, v7
	ds_read_b128 v[6:9], v213 offset:10240
	v_pk_add_f32 v[28:29], v[14:15], v[32:33]
	ds_read_b128 v[14:17], v213 offset:11264
	v_cvt_pk_bf16_f32 v2, v94, v95
	s_waitcnt lgkmcnt(1)
	v_pk_mul_f32 v[30:31], v[6:7], v[82:83]
	v_mov_b64_e32 v[152:153], s[4:5]
	v_mfma_f32_32x32x16_bf16 v[34:49], v[10:13], v[2:5], v[34:49]
	v_mul_f32_e32 v2, v8, v84
	v_mul_f32_e32 v3, v9, v85
	s_waitcnt lgkmcnt(0)
	v_mul_f32_e32 v4, v16, v88
	v_mul_f32_e32 v5, v17, v89
	v_pk_mul_f32 v[14:15], v[14:15], v[86:87]
	v_pk_fma_f32 v[8:9], v[8:9], v[84:85], v[4:5]
	v_pk_fma_f32 v[6:7], v[6:7], v[82:83], v[14:15]
	v_cvt_pk_bf16_f32 v5, v4, v5
	v_cvt_pk_bf16_f32 v3, v2, v3
	v_cvt_pk_bf16_f32 v4, v14, v15
	v_pk_add_f32 v[32:33], v[8:9], v[90:91]
	v_pk_add_f32 v[90:91], v[6:7], v[92:93]
	ds_read_b128 v[6:9], v213 offset:34816
	ds_read_b128 v[14:17], v213 offset:4096
	v_cvt_pk_bf16_f32 v2, v30, v31
	s_mov_b32 s13, 0
	s_mov_b64 s[6:7], 0
	v_mfma_f32_32x32x16_bf16 v[50:65], v[10:13], v[2:5], v[50:65]
	ds_read_b128 v[2:5], v213 offset:5120
	ds_read_b128 v[10:13], v213 offset:12288
	s_waitcnt lgkmcnt(2)
	v_pk_mul_f32 v[30:31], v[16:17], v[76:77]
	v_pk_mul_f32 v[92:93], v[14:15], v[74:75]
	s_waitcnt lgkmcnt(1)
	v_pk_mul_f32 v[4:5], v[4:5], v[80:81]
	v_pk_mul_f32 v[94:95], v[2:3], v[78:79]
	v_pk_fma_f32 v[2:3], v[16:17], v[76:77], v[4:5]
	v_cvt_pk_bf16_f32 v5, v4, v5
	v_pk_add_f32 v[96:97], v[2:3], v[26:27]
	v_cvt_pk_bf16_f32 v3, v30, v31
	v_cvt_pk_bf16_f32 v4, v94, v95
	v_cvt_pk_bf16_f32 v2, v92, v93
	v_pk_fma_f32 v[14:15], v[14:15], v[74:75], v[94:95]
	s_waitcnt lgkmcnt(0)
	v_pk_mul_f32 v[30:31], v[10:11], v[74:75]
	v_mfma_f32_32x32x16_bf16 v[34:49], v[6:9], v[2:5], v[34:49]
	ds_read_b128 v[2:5], v213 offset:13312
	v_add_f32_e32 v98, v14, v28
	v_add_f32_e32 v99, v15, v29
	ds_read_b128 v[14:17], v213 offset:35840
	v_pk_mul_f32 v[26:27], v[12:13], v[76:77]
	s_waitcnt lgkmcnt(1)
	v_pk_mul_f32 v[4:5], v[4:5], v[80:81]
	v_pk_mul_f32 v[28:29], v[2:3], v[78:79]
	v_pk_fma_f32 v[2:3], v[12:13], v[76:77], v[4:5]
	v_pk_fma_f32 v[10:11], v[10:11], v[74:75], v[28:29]
	v_pk_add_f32 v[32:33], v[2:3], v[32:33]
	v_pk_add_f32 v[92:93], v[10:11], v[90:91]
	ds_read_b128 v[10:13], v213 offset:6144
	v_cvt_pk_bf16_f32 v5, v4, v5
	v_cvt_pk_bf16_f32 v3, v26, v27
	v_cvt_pk_bf16_f32 v4, v28, v29
	ds_read_b128 v[26:29], v213 offset:7168
	v_cvt_pk_bf16_f32 v2, v30, v31
	s_waitcnt lgkmcnt(1)
	v_pk_mul_f32 v[30:31], v[10:11], v[66:67]
	v_mfma_f32_32x32x16_bf16 v[50:65], v[6:9], v[2:5], v[50:65]
	v_mul_f32_e32 v2, v12, v68
	v_mul_f32_e32 v3, v13, v69
	s_waitcnt lgkmcnt(0)
	v_mul_f32_e32 v4, v28, v72
	v_mul_f32_e32 v5, v29, v73
	v_pk_mul_f32 v[6:7], v[26:27], v[70:71]
	v_pk_fma_f32 v[8:9], v[12:13], v[68:69], v[4:5]
	v_cvt_pk_bf16_f32 v3, v2, v3
	v_pk_fma_f32 v[10:11], v[10:11], v[66:67], v[6:7]
	v_pk_add_f32 v[94:95], v[8:9], v[96:97]
	v_cvt_pk_bf16_f32 v5, v4, v5
	v_cvt_pk_bf16_f32 v4, v6, v7
	ds_read_b128 v[6:9], v213 offset:14336
	v_pk_add_f32 v[96:97], v[10:11], v[98:99]
	ds_read_b128 v[10:13], v213 offset:15360
	v_cvt_pk_bf16_f32 v2, v30, v31
	s_waitcnt lgkmcnt(1)
	v_pk_mul_f32 v[30:31], v[6:7], v[66:67]
	v_mfma_f32_32x32x16_bf16 v[34:49], v[14:17], v[2:5], v[34:49]
	s_waitcnt lgkmcnt(0)
	v_mul_f32_e32 v10, v10, v70
	v_mul_f32_e32 v11, v11, v71
	v_mul_f32_e32 v2, v8, v68
	v_mul_f32_e32 v3, v9, v69
	v_pk_mul_f32 v[4:5], v[12:13], v[72:73]
	v_pk_fma_f32 v[6:7], v[6:7], v[66:67], v[10:11]
	v_pk_fma_f32 v[8:9], v[8:9], v[68:69], v[4:5]
	v_pk_add_f32 v[92:93], v[6:7], v[92:93]
	v_cvt_pk_bf16_f32 v3, v2, v3
	v_pk_add_f32 v[90:91], v[8:9], v[32:33]
	v_cvt_pk_bf16_f32 v5, v4, v5
	v_cvt_pk_bf16_f32 v4, v10, v11
	ds_read_b128 v[26:29], v213 offset:36864
	ds_read_b128 v[6:9], v213 offset:16384
	v_cvt_pk_bf16_f32 v2, v30, v31
	ds_read_b128 v[98:101], v213 offset:25600
	ds_read_b128 v[102:105], v213 offset:37888
	v_mfma_f32_32x32x16_bf16 v[50:65], v[14:17], v[2:5], v[50:65]
	ds_read_b128 v[2:5], v213 offset:17408
	ds_read_b128 v[30:33], v213 offset:24576
	s_waitcnt lgkmcnt(4)
	v_pk_mul_f32 v[12:13], v[6:7], v[18:19]
	v_pk_mul_f32 v[10:11], v[8:9], v[20:21]
	s_waitcnt lgkmcnt(1)
	v_pk_mul_f32 v[14:15], v[2:3], v[22:23]
	v_pk_mul_f32 v[22:23], v[98:99], v[22:23]
	v_pk_fma_f32 v[112:113], v[6:7], v[18:19], v[14:15]
	s_waitcnt lgkmcnt(0)
	v_pk_mul_f32 v[114:115], v[30:31], v[18:19]
	v_pk_fma_f32 v[118:119], v[30:31], v[18:19], v[22:23]
	v_pk_mul_f32 v[4:5], v[4:5], v[24:25]
	v_pk_mul_f32 v[106:107], v[32:33], v[20:21]
	v_pk_mul_f32 v[24:25], v[100:101], v[24:25]
	ds_read_b128 v[98:101], v213 offset:18432
	v_cvt_pk_bf16_f32 v19, v106, v107
	ds_read_b128 v[106:109], v213 offset:19456
	v_pk_fma_f32 v[110:111], v[8:9], v[20:21], v[4:5]
	v_cvt_pk_bf16_f32 v5, v4, v5
	v_cvt_pk_bf16_f32 v3, v10, v11
	v_cvt_pk_bf16_f32 v4, v14, v15
	s_waitcnt lgkmcnt(0)
	v_pk_mul_f32 v[106:107], v[106:107], v[86:87]
	v_cvt_pk_bf16_f32 v2, v12, v13
	v_pk_mul_f32 v[120:121], v[98:99], v[82:83]
	v_pk_mul_f32 v[108:109], v[108:109], v[88:89]
	v_pk_fma_f32 v[98:99], v[98:99], v[82:83], v[106:107]
	v_mfma_f32_32x32x16_bf16 v[2:17], v[26:29], v[2:5], 0
	v_cvt_pk_bf16_f32 v18, v114, v115
	v_mul_f32_e32 v114, v100, v84
	v_mul_f32_e32 v115, v101, v85
	v_fma_f32 v100, v100, v84, v108
	v_fma_f32 v101, v101, v85, v109
	v_pk_add_f32 v[124:125], v[98:99], v[112:113]
	v_pk_add_f32 v[122:123], v[100:101], v[110:111]
	v_cvt_pk_bf16_f32 v101, v108, v109
	v_cvt_pk_bf16_f32 v100, v106, v107
	ds_read_b128 v[106:109], v213 offset:26624
	v_pk_fma_f32 v[116:117], v[32:33], v[20:21], v[24:25]
	v_cvt_pk_bf16_f32 v21, v24, v25
	v_cvt_pk_bf16_f32 v20, v22, v23
	ds_read_b128 v[110:113], v213 offset:27648
	v_cvt_pk_bf16_f32 v99, v114, v115
	v_mfma_f32_32x32x16_bf16 v[18:33], v[26:29], v[18:21], 0
	v_cvt_pk_bf16_f32 v98, v120, v121
	s_waitcnt lgkmcnt(1)
	v_mul_f32_e32 v114, v106, v82
	v_mul_f32_e32 v115, v107, v83
	s_waitcnt lgkmcnt(0)
	v_pk_mul_f32 v[86:87], v[110:111], v[86:87]
	v_pk_mul_f32 v[88:89], v[112:113], v[88:89]
	v_pk_fma_f32 v[82:83], v[106:107], v[82:83], v[86:87]
	v_mfma_f32_32x32x16_bf16 v[2:17], v[102:105], v[98:101], v[2:17]
	v_mul_f32_e32 v98, v108, v84
	v_mul_f32_e32 v99, v109, v85
	v_fma_f32 v84, v108, v84, v88
	v_fma_f32 v85, v109, v85, v89
	v_add_f32_e32 v108, v82, v118
	v_add_f32_e32 v109, v83, v119
	v_cvt_pk_bf16_f32 v83, v98, v99
	v_pk_add_f32 v[106:107], v[84:85], v[116:117]
	v_cvt_pk_bf16_f32 v85, v88, v89
	v_cvt_pk_bf16_f32 v84, v86, v87
	ds_read_b128 v[86:89], v213 offset:38912
	ds_read_b128 v[98:101], v213 offset:20480
	v_cvt_pk_bf16_f32 v82, v114, v115
	s_waitcnt lgkmcnt(0)
	v_pk_mul_f32 v[110:111], v[100:101], v[76:77]
	v_mfma_f32_32x32x16_bf16 v[18:33], v[102:105], v[82:85], v[18:33]
	ds_read_b128 v[82:85], v213 offset:21504
	ds_read_b128 v[102:105], v213 offset:28672
	v_mul_f32_e32 v112, v98, v74
	v_mul_f32_e32 v113, v99, v75
	s_waitcnt lgkmcnt(1)
	v_pk_mul_f32 v[84:85], v[84:85], v[80:81]
	v_pk_mul_f32 v[114:115], v[82:83], v[78:79]
	v_pk_fma_f32 v[82:83], v[100:101], v[76:77], v[84:85]
	v_cvt_pk_bf16_f32 v85, v84, v85
	v_pk_add_f32 v[116:117], v[82:83], v[122:123]
	v_cvt_pk_bf16_f32 v83, v110, v111
	v_cvt_pk_bf16_f32 v84, v114, v115
	v_cvt_pk_bf16_f32 v82, v112, v113
	v_pk_fma_f32 v[98:99], v[98:99], v[74:75], v[114:115]
	s_waitcnt lgkmcnt(0)
	v_pk_mul_f32 v[112:113], v[102:103], v[74:75]
	v_mfma_f32_32x32x16_bf16 v[2:17], v[86:89], v[82:85], v[2:17]
	ds_read_b128 v[82:85], v213 offset:29696
	v_add_f32_e32 v118, v98, v124
	v_add_f32_e32 v119, v99, v125
	v_mul_f32_e32 v110, v104, v76
	v_mul_f32_e32 v111, v105, v77
	ds_read_b128 v[98:101], v213 offset:39936
	s_waitcnt lgkmcnt(1)
	v_pk_mul_f32 v[78:79], v[82:83], v[78:79]
	v_pk_mul_f32 v[80:81], v[84:85], v[80:81]
	v_pk_fma_f32 v[74:75], v[102:103], v[74:75], v[78:79]
	v_pk_fma_f32 v[76:77], v[104:105], v[76:77], v[80:81]
	v_pk_add_f32 v[104:105], v[74:75], v[108:109]
	v_pk_add_f32 v[102:103], v[76:77], v[106:107]
	v_cvt_pk_bf16_f32 v77, v80, v81
	v_cvt_pk_bf16_f32 v76, v78, v79
	ds_read_b128 v[78:81], v213 offset:22528
	ds_read_b128 v[82:85], v213 offset:23552
	v_cvt_pk_bf16_f32 v75, v110, v111
	v_cvt_pk_bf16_f32 v74, v112, v113
	s_waitcnt lgkmcnt(0)
	v_pk_mul_f32 v[82:83], v[82:83], v[70:71]
	v_mfma_f32_32x32x16_bf16 v[18:33], v[86:89], v[74:77], v[18:33]
	v_mul_f32_e32 v74, v80, v68
	v_mul_f32_e32 v75, v81, v69
	v_mul_f32_e32 v76, v84, v72
	v_mul_f32_e32 v77, v85, v73
	v_mul_f32_e32 v86, v78, v66
	v_mul_f32_e32 v87, v79, v67
	v_pk_fma_f32 v[80:81], v[80:81], v[68:69], v[76:77]
	v_pk_fma_f32 v[78:79], v[78:79], v[66:67], v[82:83]
	v_cvt_pk_bf16_f32 v75, v74, v75
	v_pk_add_f32 v[88:89], v[80:81], v[116:117]
	v_pk_add_f32 v[106:107], v[78:79], v[118:119]
	ds_read_b128 v[78:81], v213 offset:30720
	v_cvt_pk_bf16_f32 v77, v76, v77
	v_cvt_pk_bf16_f32 v76, v82, v83
	ds_read_b128 v[82:85], v213 offset:31744
	v_cvt_pk_bf16_f32 v74, v86, v87
	s_waitcnt lgkmcnt(0)
	v_pk_mul_f32 v[72:73], v[84:85], v[72:73]
	v_mfma_f32_32x32x16_bf16 v[2:17], v[98:101], v[74:77], v[2:17]
	v_mul_f32_e32 v74, v80, v68
	v_mul_f32_e32 v75, v81, v69
	v_fma_f32 v68, v80, v68, v72
	v_fma_f32 v69, v81, v69, v73
	v_mul_f32_e32 v70, v82, v70
	v_mul_f32_e32 v71, v83, v71
	v_pk_add_f32 v[84:85], v[68:69], v[102:103]
	v_cvt_pk_bf16_f32 v69, v72, v73
	v_pk_mov_b32 v[72:73], v[96:97], v[94:95] op_sel:[1,0]
	v_mov_b32_e32 v97, v95
	v_pk_add_f32 v[72:73], v[72:73], v[96:97]
	v_pk_mul_f32 v[76:77], v[78:79], v[66:67]
	v_pk_fma_f32 v[66:67], v[78:79], v[66:67], v[70:71]
	v_pk_add_f32 v[72:73], v[72:73], v[72:73] op_sel:[0,1] op_sel_hi:[1,0]
	v_pk_add_f32 v[86:87], v[66:67], v[104:105]
	v_mov_b32_e32 v66, v72
	s_nop 1
	v_permlane32_swap_b32_e32 v72, v66
	v_add_f32_e32 v66, v72, v66
	v_cvt_pk_bf16_f32 v67, v74, v75
	v_rcp_f32_e32 v74, v66
	v_cvt_pk_bf16_f32 v68, v70, v71
	v_cvt_pk_bf16_f32 v66, v76, v77
	v_pk_mul_f32 v[70:71], v[46:47], v[74:75] op_sel_hi:[1,0]
	s_nop 0
	v_mfma_f32_32x32x16_bf16 v[18:33], v[98:101], v[66:69], v[18:33]
	v_mul_f32_e32 v66, v42, v74
	v_mul_f32_e32 v67, v43, v74
	v_pk_mov_b32 v[42:43], v[92:93], v[90:91] op_sel:[1,0]
	v_mov_b32_e32 v93, v91
	v_pk_add_f32 v[42:43], v[42:43], v[92:93]
	v_pk_mul_f32 v[68:69], v[44:45], v[74:75] op_sel_hi:[1,0]
	v_pk_add_f32 v[42:43], v[42:43], v[42:43] op_sel:[0,1] op_sel_hi:[1,0]
	v_pk_mov_b32 v[44:45], v[106:107], v[88:89] op_sel:[1,0]
	v_mov_b32_e32 v43, v42
	s_nop 1
	v_permlane32_swap_b32_e32 v42, v43
	v_add_f32_e32 v42, v42, v43
	v_rcp_f32_e32 v42, v42
	v_mov_b32_e32 v107, v89
	v_pk_add_f32 v[44:45], v[44:45], v[106:107]
	v_pk_mul_f32 v[72:73], v[48:49], v[74:75] op_sel_hi:[1,0]
	v_pk_add_f32 v[44:45], v[44:45], v[44:45] op_sel:[0,1] op_sel_hi:[1,0]
	v_pk_mul_f32 v[36:37], v[36:37], v[74:75] op_sel_hi:[1,0]
	v_pk_mul_f32 v[38:39], v[38:39], v[74:75] op_sel_hi:[1,0]
	v_pk_mul_f32 v[40:41], v[40:41], v[74:75] op_sel_hi:[1,0]
	v_pk_mul_f32 v[34:35], v[34:35], v[74:75] op_sel_hi:[1,0]
	v_pk_mul_f32 v[74:75], v[58:59], v[42:43] op_sel_hi:[1,0]
	v_pk_mul_f32 v[78:79], v[60:61], v[42:43] op_sel_hi:[1,0]
	v_pk_mul_f32 v[80:81], v[62:63], v[42:43] op_sel_hi:[1,0]
	v_pk_mul_f32 v[82:83], v[64:65], v[42:43] op_sel_hi:[1,0]
	v_pk_mul_f32 v[92:93], v[52:53], v[42:43] op_sel_hi:[1,0]
	v_mov_b32_e32 v43, v44
	s_nop 1
	v_permlane32_swap_b32_e32 v44, v43
	v_add_f32_e32 v43, v44, v43
	v_rcp_f32_e32 v76, v43
	v_pk_mul_f32 v[96:97], v[54:55], v[42:43] op_sel_hi:[1,0]
	v_pk_mul_f32 v[94:95], v[56:57], v[42:43] op_sel_hi:[1,0]
	v_pk_mul_f32 v[98:99], v[50:51], v[42:43] op_sel_hi:[1,0]
	v_pk_mul_f32 v[100:101], v[4:5], v[76:77] op_sel_hi:[1,0]
	v_pk_mov_b32 v[4:5], v[86:87], v[84:85] op_sel:[1,0]
	v_mov_b32_e32 v87, v85
	v_pk_add_f32 v[4:5], v[4:5], v[86:87]
	v_pk_mul_f32 v[102:103], v[6:7], v[76:77] op_sel_hi:[1,0]
	v_pk_add_f32 v[104:105], v[4:5], v[4:5] op_sel:[0,1] op_sel_hi:[1,0]
	v_cvt_pk_bf16_f32 v7, v40, v41
	ds_read_b128 v[84:87], v150 offset:52224
	ds_read_b128 v[50:53], v150 offset:35840
	ds_read_b128 v[54:57], v150 offset:36864
	ds_read_b128 v[58:61], v150 offset:37888
	ds_read_b128 v[62:65], v150 offset:38912
	v_cvt_pk_bf16_f32 v6, v38, v39
	v_cvt_pk_bf16_f32 v5, v36, v37
	v_cvt_pk_bf16_f32 v4, v34, v35
	ds_read_b128 v[88:91], v150 offset:53248
	ds_read_b128 v[34:37], v150 offset:39936
	ds_read_b128 v[38:41], v150 offset:40960
	ds_read_b128 v[42:45], v150 offset:41984
	ds_read_b128 v[46:49], v150 offset:43008
	v_cvt_pk_bf16_f32 v95, v94, v95
	v_cvt_pk_bf16_f32 v94, v96, v97
	v_cvt_pk_bf16_f32 v93, v92, v93
	v_cvt_pk_bf16_f32 v92, v98, v99
	s_waitcnt lgkmcnt(5)
	v_mfma_f32_32x32x16_bf16 v[50:65], v[84:87], v[4:7], v[50:65]
	v_mul_f32_e32 v10, v10, v76
	v_mul_f32_e32 v11, v11, v76
	v_mul_f32_e32 v12, v12, v76
	v_mul_f32_e32 v13, v13, v76
	v_mul_f32_e32 v8, v8, v76
	v_mul_f32_e32 v9, v9, v76
	v_mov_b32_e32 v77, v104
	s_nop 1
	v_permlane32_swap_b32_e32 v104, v77
	v_cvt_pk_bf16_f32 v73, v72, v73
	s_waitcnt lgkmcnt(0)
	v_mfma_f32_32x32x16_bf16 v[34:49], v[84:87], v[92:95], v[34:49]
	v_cvt_pk_bf16_f32 v72, v70, v71
	v_cvt_pk_bf16_f32 v70, v66, v67
	v_add_f32_e32 v66, v104, v77
	v_cvt_pk_bf16_f32 v71, v68, v69
	v_rcp_f32_e32 v104, v66
	v_cvt_pk_bf16_f32 v69, v82, v83
	v_cvt_pk_bf16_f32 v68, v80, v81
	v_cvt_pk_bf16_f32 v67, v78, v79
	v_cvt_pk_bf16_f32 v66, v74, v75
	ds_read_b128 v[78:81], v150 offset:54272
	v_mfma_f32_32x32x16_bf16 v[50:65], v[88:91], v[70:73], v[50:65]
	v_mul_f32_e32 v2, v2, v76
	v_mul_f32_e32 v3, v3, v76
	v_mul_f32_e32 v20, v20, v104
	v_mul_f32_e32 v21, v21, v104
	v_cvt_pk_bf16_f32 v85, v8, v9
	v_cvt_pk_bf16_f32 v82, v2, v3
	v_pk_mul_f32 v[2:3], v[22:23], v[104:105] op_sel_hi:[1,0]
	v_pk_mul_f32 v[8:9], v[24:25], v[104:105] op_sel_hi:[1,0]
	v_pk_mul_f32 v[18:19], v[18:19], v[104:105] op_sel_hi:[1,0]
	v_mfma_f32_32x32x16_bf16 v[34:49], v[88:91], v[66:69], v[34:49]
	v_cvt_pk_bf16_f32 v84, v102, v103
	v_cvt_pk_bf16_f32 v83, v100, v101
	ds_read_b128 v[86:89], v150 offset:55296
	v_cvt_pk_bf16_f32 v99, v8, v9
	v_cvt_pk_bf16_f32 v98, v2, v3
	v_cvt_pk_bf16_f32 v97, v20, v21
	v_cvt_pk_bf16_f32 v96, v18, v19
	s_waitcnt lgkmcnt(1)
	v_mfma_f32_32x32x16_bf16 v[50:65], v[78:81], v[82:85], v[50:65]
	v_mul_f32_e32 v2, v14, v76
	v_mul_f32_e32 v3, v15, v76
	v_mul_f32_e32 v8, v16, v76
	v_mul_f32_e32 v9, v17, v76
	v_mul_f32_e32 v14, v26, v104
	v_mul_f32_e32 v15, v27, v104
	v_cvt_pk_bf16_f32 v77, v8, v9
	v_cvt_pk_bf16_f32 v76, v2, v3
	v_cvt_pk_bf16_f32 v74, v10, v11
	v_pk_mul_f32 v[2:3], v[28:29], v[104:105] op_sel_hi:[1,0]
	v_mfma_f32_32x32x16_bf16 v[34:49], v[78:81], v[96:99], v[34:49]
	v_mul_f32_e32 v8, v30, v104
	v_mul_f32_e32 v9, v31, v104
	v_mul_f32_e32 v10, v32, v104
	v_mul_f32_e32 v11, v33, v104
	v_cvt_pk_bf16_f32 v75, v12, v13
	v_cvt_pk_bf16_f32 v81, v10, v11
	v_cvt_pk_bf16_f32 v80, v8, v9
	v_cvt_pk_bf16_f32 v79, v2, v3
	v_cvt_pk_bf16_f32 v78, v14, v15
	s_waitcnt lgkmcnt(0)
	v_mfma_f32_32x32x16_bf16 v[50:65], v[86:89], v[74:77], v[50:65]
	v_mfma_f32_32x32x16_bf16 v[34:49], v[86:89], v[78:81], v[34:49]
	ds_read_b128 v[86:89], v150 offset:56320
	ds_read_b128 v[18:21], v150 offset:44032
	ds_read_b128 v[22:25], v150 offset:45056
	ds_read_b128 v[26:29], v150 offset:46080
	ds_read_b128 v[30:33], v150 offset:47104
	ds_read_b128 v[100:103], v150 offset:57344
	s_waitcnt lgkmcnt(1)
	v_mfma_f32_32x32x16_bf16 v[18:33], v[86:89], v[4:7], v[18:33]
	ds_read_b128 v[2:5], v150 offset:48128
	ds_read_b128 v[6:9], v150 offset:49152
	ds_read_b128 v[10:13], v150 offset:50176
	ds_read_b128 v[14:17], v150 offset:51200
	s_waitcnt lgkmcnt(0)
	v_mfma_f32_32x32x16_bf16 v[2:17], v[86:89], v[92:95], v[2:17]
	v_mfma_f32_32x32x16_bf16 v[18:33], v[100:103], v[70:73], v[18:33]
	v_mfma_f32_32x32x16_bf16 v[2:17], v[100:103], v[66:69], v[2:17]
	ds_read_b128 v[66:69], v150 offset:58368
	ds_read_b128 v[70:73], v150 offset:59392
	s_waitcnt lgkmcnt(1)
	v_mfma_f32_32x32x16_bf16 v[18:33], v[66:69], v[82:85], v[18:33]
	v_mfma_f32_32x32x16_bf16 v[2:17], v[66:69], v[96:99], v[2:17]
	s_waitcnt lgkmcnt(0)
	v_mfma_f32_32x32x16_bf16 v[18:33], v[70:73], v[74:77], v[18:33]
	v_mfma_f32_32x32x16_bf16 v[2:17], v[70:73], v[78:81], v[2:17]
	s_nop 10
	v_mul_f32_e32 v66, v22, v22
	v_mul_f32_e32 v67, v23, v23
	v_mul_f32_e32 v68, v30, v30
	v_mul_f32_e32 v69, v31, v31
	v_mul_f32_e32 v70, v24, v24
	v_mul_f32_e32 v71, v25, v25
	v_pk_mul_f32 v[72:73], v[32:33], v[32:33]
	v_pk_mul_f32 v[74:75], v[20:21], v[20:21]
	v_pk_mul_f32 v[76:77], v[28:29], v[28:29]
	v_pk_mul_f32 v[78:79], v[26:27], v[26:27]
	v_pk_mul_f32 v[80:81], v[18:19], v[18:19]
	v_pk_fma_f32 v[78:79], v[58:59], v[58:59], v[78:79]
	v_pk_fma_f32 v[76:77], v[60:61], v[60:61], v[76:77]
	v_pk_fma_f32 v[74:75], v[52:53], v[52:53], v[74:75]
	v_pk_fma_f32 v[72:73], v[64:65], v[64:65], v[72:73]
	v_pk_fma_f32 v[70:71], v[56:57], v[56:57], v[70:71]
	v_pk_fma_f32 v[68:69], v[62:63], v[62:63], v[68:69]
	v_pk_fma_f32 v[66:67], v[54:55], v[54:55], v[66:67]
	v_pk_fma_f32 v[80:81], v[50:51], v[50:51], v[80:81]
	v_pk_add_f32 v[66:67], v[66:67], v[68:69]
	v_pk_add_f32 v[68:69], v[70:71], v[72:73]
	v_pk_add_f32 v[70:71], v[74:75], v[76:77]
	v_pk_add_f32 v[72:73], v[80:81], v[78:79]
	v_pk_add_f32 v[68:69], v[70:71], v[68:69]
	v_pk_add_f32 v[66:67], v[72:73], v[66:67]
	v_pk_mul_f32 v[72:73], v[14:15], v[14:15]
	v_pk_mov_b32 v[70:71], v[66:67], v[68:69] op_sel:[1,0]
	v_mov_b32_e32 v67, v69
	v_pk_add_f32 v[66:67], v[70:71], v[66:67]
	v_pk_mul_f32 v[70:71], v[6:7], v[6:7]
	v_pk_mul_f32 v[74:75], v[8:9], v[8:9]
	v_pk_mul_f32 v[76:77], v[16:17], v[16:17]
	v_pk_mul_f32 v[78:79], v[4:5], v[4:5]
	v_pk_mul_f32 v[80:81], v[12:13], v[12:13]
	v_pk_mul_f32 v[82:83], v[10:11], v[10:11]
	v_pk_mul_f32 v[84:85], v[2:3], v[2:3]
	v_pk_fma_f32 v[82:83], v[42:43], v[42:43], v[82:83]
	v_pk_fma_f32 v[80:81], v[44:45], v[44:45], v[80:81]
	v_pk_fma_f32 v[78:79], v[36:37], v[36:37], v[78:79]
	v_pk_fma_f32 v[76:77], v[48:49], v[48:49], v[76:77]
	v_pk_fma_f32 v[74:75], v[40:41], v[40:41], v[74:75]
	v_pk_fma_f32 v[72:73], v[46:47], v[46:47], v[72:73]
	v_pk_fma_f32 v[70:71], v[38:39], v[38:39], v[70:71]
	v_pk_fma_f32 v[84:85], v[34:35], v[34:35], v[84:85]
	v_pk_add_f32 v[70:71], v[70:71], v[72:73]
	v_pk_add_f32 v[72:73], v[74:75], v[76:77]
	v_pk_add_f32 v[74:75], v[78:79], v[80:81]
	v_pk_add_f32 v[76:77], v[84:85], v[82:83]
	v_pk_add_f32 v[72:73], v[74:75], v[72:73]
	v_pk_add_f32 v[70:71], v[76:77], v[70:71]
	v_pk_add_f32 v[66:67], v[66:67], v[66:67] op_sel:[0,1] op_sel_hi:[1,0]
	v_pk_mov_b32 v[74:75], v[70:71], v[72:73] op_sel:[1,0]
	v_mov_b32_e32 v71, v73
	v_pk_add_f32 v[70:71], v[74:75], v[70:71]
	v_mov_b32_e32 v69, v66
	v_pk_add_f32 v[70:71], v[70:71], v[70:71] op_sel:[0,1] op_sel_hi:[1,0]
	s_nop 0
	v_permlane32_swap_b32_e32 v66, v69
	v_mov_b32_e32 v68, v70
	s_nop 1
	v_permlane32_swap_b32_e32 v70, v68
	v_mov_b32_e32 v71, v66
	v_pk_add_f32 v[66:67], v[70:71], v[68:69]
	v_pk_fma_f32 v[66:67], v[66:67], s[0:1], v[152:153] op_sel_hi:[1,0,0]
	s_mov_b32 s1, 0x800000
	v_mul_f32_e32 v68, 0x4b800000, v67
	v_cmp_gt_f32_e32 vcc, s1, v67
	s_nop 1
	v_cndmask_b32_e32 v67, v67, v68, vcc
	v_rsq_f32_e32 v67, v67
	s_nop 0
	v_mul_f32_e32 v68, 0x45800000, v67
	v_cndmask_b32_e32 v68, v67, v68, vcc
	v_pk_mul_f32 v[158:159], v[50:51], v[68:69] op_sel_hi:[1,0]
	v_pk_mul_f32 v[50:51], v[18:19], v[68:69] op_sel_hi:[1,0]
	v_mul_f32_e32 v18, 0x4b800000, v66
	v_cmp_gt_f32_e32 vcc, s1, v66
	v_pk_mul_f32 v[80:81], v[60:61], v[68:69] op_sel_hi:[1,0]
	v_pk_mul_f32 v[60:61], v[28:29], v[68:69] op_sel_hi:[1,0]
	v_cndmask_b32_e32 v18, v66, v18, vcc
	v_rsq_f32_e32 v18, v18
	v_pk_mul_f32 v[78:79], v[58:59], v[68:69] op_sel_hi:[1,0]
	v_pk_mul_f32 v[160:161], v[52:53], v[68:69] op_sel_hi:[1,0]
	v_pk_mul_f32 v[82:83], v[54:55], v[68:69] op_sel_hi:[1,0]
	v_mul_f32_e32 v19, 0x45800000, v18
	v_cndmask_b32_e32 v28, v18, v19, vcc
	v_pk_mul_f32 v[168:169], v[56:57], v[68:69] op_sel_hi:[1,0]
	v_pk_mul_f32 v[58:59], v[26:27], v[68:69] op_sel_hi:[1,0]
	v_pk_mul_f32 v[52:53], v[20:21], v[68:69] op_sel_hi:[1,0]
	v_pk_mul_f32 v[54:55], v[22:23], v[68:69] op_sel_hi:[1,0]
	v_pk_mul_f32 v[56:57], v[24:25], v[68:69] op_sel_hi:[1,0]
	v_pk_mul_f32 v[18:19], v[42:43], v[28:29] op_sel_hi:[1,0]
	v_pk_mul_f32 v[20:21], v[44:45], v[28:29] op_sel_hi:[1,0]
	v_pk_mul_f32 v[22:23], v[46:47], v[28:29] op_sel_hi:[1,0]
	v_pk_mul_f32 v[26:27], v[48:49], v[28:29] op_sel_hi:[1,0]
	v_pk_mul_f32 v[162:163], v[34:35], v[28:29] op_sel_hi:[1,0]
	v_pk_mul_f32 v[164:165], v[36:37], v[28:29] op_sel_hi:[1,0]
	v_pk_mul_f32 v[166:167], v[38:39], v[28:29] op_sel_hi:[1,0]
	v_pk_mul_f32 v[24:25], v[40:41], v[28:29] op_sel_hi:[1,0]
	v_pk_mul_f32 v[104:105], v[2:3], v[28:29] op_sel_hi:[1,0]
	v_pk_mul_f32 v[112:113], v[4:5], v[28:29] op_sel_hi:[1,0]
	ds_read_b128 v[2:5], v150 offset:60416
	ds_read_b128 v[34:37], v174 offset:32768
	ds_read_b128 v[38:41], v174 offset:32800
	ds_read_b128 v[42:45], v174 offset:32832
	ds_read_b128 v[46:49], v174 offset:32864
	v_cvt_pk_bf16_f32 v129, v168, v169
	v_cvt_pk_bf16_f32 v128, v82, v83
	v_cvt_pk_bf16_f32 v127, v160, v161
	v_cvt_pk_bf16_f32 v126, v158, v159
	v_cvt_pk_bf16_f32 v137, v24, v25
	v_cvt_pk_bf16_f32 v136, v166, v167
	v_cvt_pk_bf16_f32 v135, v164, v165
	s_waitcnt lgkmcnt(0)
	v_mfma_f32_32x32x16_bf16 v[86:101], v[2:5], v[126:129], v[34:49]
	v_cvt_pk_bf16_f32 v134, v162, v163
	v_mul_f32_e32 v84, v62, v68
	v_mul_f32_e32 v85, v63, v68
	v_mul_f32_e32 v170, v64, v68
	v_mul_f32_e32 v171, v65, v68
	v_pk_mul_f32 v[62:63], v[30:31], v[68:69] op_sel_hi:[1,0]
	v_pk_mul_f32 v[64:65], v[32:33], v[68:69] op_sel_hi:[1,0]
	v_pk_mul_f32 v[116:117], v[6:7], v[28:29] op_sel_hi:[1,0]
	v_pk_mul_f32 v[154:155], v[8:9], v[28:29] op_sel_hi:[1,0]
	v_mfma_f32_32x32x16_bf16 v[34:49], v[2:5], v[134:137], v[34:49]
	ds_read_b128 v[6:9], v150 offset:61440
	ds_read_b128 v[66:69], v174 offset:32896
	ds_read_b128 v[106:109], v150 offset:64512
	v_cvt_pk_bf16_f32 v125, v170, v171
	v_cvt_pk_bf16_f32 v124, v84, v85
	v_cvt_pk_bf16_f32 v123, v80, v81
	v_cvt_pk_bf16_f32 v122, v78, v79
	v_cvt_pk_bf16_f32 v149, v26, v27
	v_cvt_pk_bf16_f32 v148, v22, v23
	v_cvt_pk_bf16_f32 v147, v20, v21
	v_cvt_pk_bf16_f32 v146, v18, v19
	s_waitcnt lgkmcnt(2)
	v_mfma_f32_32x32x16_bf16 v[86:101], v[6:9], v[122:125], v[86:101]
	v_mul_f32_e32 v102, v10, v28
	v_mul_f32_e32 v103, v11, v28
	v_mul_f32_e32 v110, v12, v28
	v_mul_f32_e32 v111, v13, v28
	v_mul_f32_e32 v114, v14, v28
	v_mul_f32_e32 v115, v15, v28
	v_pk_mul_f32 v[156:157], v[16:17], v[28:29] op_sel_hi:[1,0]
	ds_read_b128 v[176:179], v174 offset:33536
	ds_read_b128 v[180:183], v174 offset:33568
	ds_read_b128 v[184:187], v174 offset:33600
	ds_read_b128 v[28:31], v174 offset:33632
	ds_read_b128 v[188:191], v174 offset:33792
	ds_read_b128 v[192:195], v174 offset:33824
	ds_read_b128 v[196:199], v174 offset:33856
	ds_read_b128 v[200:203], v174 offset:33888
	ds_read_b128 v[204:207], v150 offset:62464
	v_cvt_pk_bf16_f32 v133, v56, v57
	v_mfma_f32_32x32x16_bf16 v[34:49], v[6:9], v[146:149], v[34:49]
	v_cvt_pk_bf16_f32 v132, v54, v55
	v_cvt_pk_bf16_f32 v131, v52, v53
	v_cvt_pk_bf16_f32 v130, v50, v51
	ds_read_b128 v[70:73], v174 offset:33664
	ds_read_b128 v[74:77], v174 offset:33920
	ds_read_b128 v[208:211], v150 offset:63488
	v_cvt_pk_bf16_f32 v145, v154, v155
	v_cvt_pk_bf16_f32 v144, v116, v117
	v_cvt_pk_bf16_f32 v143, v112, v113
	v_cvt_pk_bf16_f32 v142, v104, v105
	s_waitcnt lgkmcnt(3)
	v_mfma_f32_32x32x16_bf16 v[86:101], v[204:207], v[130:133], v[86:101]
	v_cvt_pk_bf16_f32 v121, v64, v65
	v_cvt_pk_bf16_f32 v120, v62, v63
	v_cvt_pk_bf16_f32 v119, v60, v61
	v_cvt_pk_bf16_f32 v118, v58, v59
	v_cvt_pk_bf16_f32 v141, v156, v157
	v_cvt_pk_bf16_f32 v140, v114, v115
	v_cvt_pk_bf16_f32 v139, v110, v111
	v_mfma_f32_32x32x16_bf16 v[34:49], v[204:207], v[142:145], v[34:49]
	v_cvt_pk_bf16_f32 v138, v102, v103
	v_fma_f32 v16, v30, v170, v202
	v_fma_f32 v17, v31, v171, v203
	v_fma_f32 v14, v28, v84, v200
	v_fma_f32 v15, v29, v85, v201
	v_pk_fma_f32 v[12:13], v[186:187], v[80:81], v[198:199]
	v_pk_fma_f32 v[10:11], v[184:185], v[78:79], v[196:197]
	v_pk_fma_f32 v[8:9], v[182:183], v[168:169], v[194:195]
	s_waitcnt lgkmcnt(0)
	v_mfma_f32_32x32x16_bf16 v[86:101], v[208:211], v[118:121], v[86:101]
	v_fma_f32 v6, v180, v82, v192
	v_fma_f32 v7, v181, v83, v193
	ds_read_b128 v[78:81], v174 offset:33760
	ds_read_b128 v[82:85], v174 offset:33248
	v_fma_f32 v4, v178, v160, v190
	v_fma_f32 v5, v179, v161, v191
	v_pk_fma_f32 v[2:3], v[176:177], v[158:159], v[188:189]
	v_pk_fma_f32 v[32:33], v[30:31], v[26:27], v[202:203]
	v_pk_fma_f32 v[30:31], v[28:29], v[22:23], v[200:201]
	v_pk_fma_f32 v[28:29], v[186:187], v[20:21], v[198:199]
	v_pk_fma_f32 v[26:27], v[184:185], v[18:19], v[196:197]
	v_pk_fma_f32 v[24:25], v[182:183], v[24:25], v[194:195]
	v_pk_fma_f32 v[22:23], v[180:181], v[166:167], v[192:193]
	v_pk_fma_f32 v[20:21], v[178:179], v[164:165], v[190:191]
	v_pk_fma_f32 v[18:19], v[176:177], v[162:163], v[188:189]
	ds_read_b128 v[158:161], v174 offset:33696
	ds_read_b128 v[162:165], v174 offset:33728
	ds_read_b128 v[166:169], v174 offset:33952
	ds_read_b128 v[176:179], v174 offset:33984
	ds_read_b128 v[180:183], v174 offset:34016
	ds_read_b128 v[184:187], v212 offset:11264
	v_mfma_f32_32x32x16_bf16 v[34:49], v[208:211], v[138:141], v[34:49]
	v_cvt_pk_bf16_f32 v86, v86, v87
	v_cvt_pk_bf16_f32 v87, v88, v89
	v_cvt_pk_bf16_f32 v88, v90, v91
	v_cvt_pk_bf16_f32 v89, v92, v93
	ds_read_b128 v[90:93], v212 offset:12288
	v_pk_max_i16 v86, v86, 0
	v_pk_max_i16 v87, v87, 0
	v_pk_max_i16 v88, v88, 0
	v_pk_max_i16 v89, v89, 0
	s_nop 1
	s_nop 0
	v_cvt_pk_bf16_f32 v188, v34, v35
	v_cvt_pk_bf16_f32 v189, v36, v37
	v_cvt_pk_bf16_f32 v190, v38, v39
	v_cvt_pk_bf16_f32 v191, v40, v41
	s_waitcnt lgkmcnt(1)
	v_mfma_f32_32x32x16_bf16 v[2:17], v[184:187], v[86:89], v[2:17]
	v_pk_max_i16 v188, v188, 0
	v_pk_max_i16 v189, v189, 0
	v_pk_max_i16 v190, v190, 0
	v_pk_max_i16 v191, v191, 0
	v_cvt_pk_bf16_f32 v94, v94, v95
	v_cvt_pk_bf16_f32 v95, v96, v97
	v_cvt_pk_bf16_f32 v96, v98, v99
	v_cvt_pk_bf16_f32 v97, v100, v101
	v_cvt_pk_bf16_f32 v98, v42, v43
	v_cvt_pk_bf16_f32 v99, v44, v45
	v_mfma_f32_32x32x16_bf16 v[18:33], v[184:187], v[188:191], v[18:33]
	ds_read_b128 v[184:187], v212 offset:19456
	v_cvt_pk_bf16_f32 v100, v46, v47
	v_cvt_pk_bf16_f32 v101, v48, v49
	v_fma_f32 v64, v80, v64, v182
	v_fma_f32 v65, v81, v65, v183
	v_pk_fma_f32 v[62:63], v[78:79], v[62:63], v[180:181]
	v_pk_fma_f32 v[60:61], v[164:165], v[60:61], v[178:179]
	v_pk_fma_f32 v[58:59], v[162:163], v[58:59], v[176:177]
	v_pk_max_i16 v94, v94, 0
	v_pk_max_i16 v95, v95, 0
	v_pk_max_i16 v96, v96, 0
	v_pk_max_i16 v97, v97, 0
	v_pk_max_i16 v98, v98, 0
	v_pk_max_i16 v99, v99, 0
	v_pk_max_i16 v100, v100, 0
	v_pk_max_i16 v101, v101, 0
	v_pk_fma_f32 v[56:57], v[160:161], v[56:57], v[168:169]
	s_waitcnt lgkmcnt(1)
	v_mfma_f32_32x32x16_bf16 v[2:17], v[90:93], v[94:97], v[2:17]
	v_fma_f32 v54, v158, v54, v166
	v_fma_f32 v55, v159, v55, v167
	v_fma_f32 v52, v72, v52, v76
	v_fma_f32 v53, v73, v53, v77
	v_fma_f32 v50, v70, v50, v74
	v_fma_f32 v51, v71, v51, v75
	v_pk_fma_f32 v[48:49], v[80:81], v[156:157], v[182:183]
	v_pk_fma_f32 v[46:47], v[78:79], v[114:115], v[180:181]
	v_pk_fma_f32 v[44:45], v[164:165], v[110:111], v[178:179]
	v_pk_fma_f32 v[42:43], v[162:163], v[102:103], v[176:177]
	v_mfma_f32_32x32x16_bf16 v[18:33], v[90:93], v[98:101], v[18:33]
	ds_read_b128 v[90:93], v212 offset:20480
	v_fma_f32 v40, v160, v154, v168
	v_fma_f32 v41, v161, v155, v169
	v_fma_f32 v38, v158, v116, v166
	v_fma_f32 v39, v159, v117, v167
	v_pk_fma_f32 v[36:37], v[72:73], v[112:113], v[76:77]
	v_pk_fma_f32 v[34:35], v[70:71], v[104:105], v[74:75]
	s_waitcnt lgkmcnt(1)
	v_mfma_f32_32x32x16_bf16 v[50:65], v[184:187], v[86:89], v[50:65]
	ds_read_b128 v[70:73], v174 offset:32928
	ds_read_b128 v[74:77], v174 offset:32960
	ds_read_b128 v[78:81], v174 offset:32992
	ds_read_b128 v[86:89], v174 offset:33024
	ds_read_b128 v[110:113], v212 offset:1024
	v_mfma_f32_32x32x16_bf16 v[34:49], v[184:187], v[188:191], v[34:49]
	s_waitcnt lgkmcnt(5)
	v_mfma_f32_32x32x16_bf16 v[50:65], v[90:93], v[94:97], v[50:65]
	v_mfma_f32_32x32x16_bf16 v[34:49], v[90:93], v[98:101], v[34:49]
	s_waitcnt lgkmcnt(2)
	v_mfma_f32_32x32x16_bf16 v[90:105], v[106:109], v[126:129], v[66:81]
	v_mfma_f32_32x32x16_bf16 v[66:81], v[106:109], v[134:137], v[66:81]
	ds_read_b128 v[106:109], v212 offset:0
	s_waitcnt lgkmcnt(0)
	v_mfma_f32_32x32x16_bf16 v[90:105], v[106:109], v[122:125], v[90:105]
	v_mfma_f32_32x32x16_bf16 v[66:81], v[106:109], v[146:149], v[66:81]
	ds_read_b128 v[106:109], v212 offset:2048
	v_mfma_f32_32x32x16_bf16 v[90:105], v[110:113], v[130:133], v[90:105]
	v_mfma_f32_32x32x16_bf16 v[66:81], v[110:113], v[142:145], v[66:81]
	ds_read_b128 v[110:113], v212 offset:13312
	s_waitcnt lgkmcnt(1)
	v_mfma_f32_32x32x16_bf16 v[90:105], v[106:109], v[118:121], v[90:105]
	v_mfma_f32_32x32x16_bf16 v[66:81], v[106:109], v[138:141], v[66:81]
	s_nop 10
	v_cvt_pk_bf16_f32 v90, v90, v91
	v_cvt_pk_bf16_f32 v91, v92, v93
	v_cvt_pk_bf16_f32 v92, v94, v95
	v_cvt_pk_bf16_f32 v94, v98, v99
	v_cvt_pk_bf16_f32 v95, v100, v101
	ds_read_b128 v[98:101], v212 offset:21504
	v_cvt_pk_bf16_f32 v66, v66, v67
	v_cvt_pk_bf16_f32 v67, v68, v69
	v_cvt_pk_bf16_f32 v68, v70, v71
	v_cvt_pk_bf16_f32 v93, v96, v97
	v_cvt_pk_bf16_f32 v69, v72, v73
	ds_read_b128 v[70:73], v212 offset:14336
	v_pk_max_i16 v90, v90, 0
	v_pk_max_i16 v91, v91, 0
	v_pk_max_i16 v92, v92, 0
	v_pk_max_i16 v93, v93, 0
	v_pk_max_i16 v66, v66, 0
	v_pk_max_i16 v67, v67, 0
	v_pk_max_i16 v68, v68, 0
	v_pk_max_i16 v69, v69, 0
	v_cvt_pk_bf16_f32 v96, v102, v103
	s_waitcnt lgkmcnt(2)
	v_mfma_f32_32x32x16_bf16 v[2:17], v[110:113], v[90:93], v[2:17]
	v_cvt_pk_bf16_f32 v97, v104, v105
	v_cvt_pk_bf16_f32 v74, v74, v75
	v_cvt_pk_bf16_f32 v75, v76, v77
	v_cvt_pk_bf16_f32 v76, v78, v79
	v_cvt_pk_bf16_f32 v77, v80, v81
	v_pk_max_i16 v94, v94, 0
	v_pk_max_i16 v95, v95, 0
	v_pk_max_i16 v96, v96, 0
	v_pk_max_i16 v97, v97, 0
	v_pk_max_i16 v74, v74, 0
	v_pk_max_i16 v75, v75, 0
	v_pk_max_i16 v76, v76, 0
	v_pk_max_i16 v77, v77, 0
	v_mfma_f32_32x32x16_bf16 v[18:33], v[110:113], v[66:69], v[18:33]
	s_waitcnt lgkmcnt(1)
	v_mfma_f32_32x32x16_bf16 v[34:49], v[98:101], v[66:69], v[34:49]
	ds_read_b128 v[66:69], v212 offset:22528
	v_mfma_f32_32x32x16_bf16 v[50:65], v[98:101], v[90:93], v[50:65]
	s_waitcnt lgkmcnt(1)
	v_mfma_f32_32x32x16_bf16 v[2:17], v[70:73], v[94:97], v[2:17]
	v_mfma_f32_32x32x16_bf16 v[18:33], v[70:73], v[74:77], v[18:33]
	ds_read_b128 v[78:81], v212 offset:3072
	s_waitcnt lgkmcnt(1)
	v_mfma_f32_32x32x16_bf16 v[50:65], v[66:69], v[94:97], v[50:65]
	ds_read_b128 v[90:93], v174 offset:33056
	ds_read_b128 v[94:97], v174 offset:33088
	ds_read_b128 v[98:101], v174 offset:33120
	ds_read_b128 v[70:73], v174 offset:33152
	v_mfma_f32_32x32x16_bf16 v[34:49], v[66:69], v[74:77], v[34:49]
	ds_read_b128 v[66:69], v212 offset:4096
	ds_read_b128 v[74:77], v212 offset:5120
	s_waitcnt lgkmcnt(3)
	v_mfma_f32_32x32x16_bf16 v[102:117], v[78:81], v[126:129], v[86:101]
	v_mfma_f32_32x32x16_bf16 v[86:101], v[78:81], v[134:137], v[86:101]
	s_waitcnt lgkmcnt(1)
	v_mfma_f32_32x32x16_bf16 v[86:101], v[66:69], v[146:149], v[86:101]
	v_mfma_f32_32x32x16_bf16 v[102:117], v[66:69], v[122:125], v[102:117]
	ds_read_b128 v[66:69], v212 offset:6144
	s_waitcnt lgkmcnt(1)
	v_mfma_f32_32x32x16_bf16 v[86:101], v[74:77], v[142:145], v[86:101]
	v_mfma_f32_32x32x16_bf16 v[102:117], v[74:77], v[130:133], v[102:117]
	ds_read_b128 v[74:77], v212 offset:15360
	s_waitcnt lgkmcnt(1)
	v_mfma_f32_32x32x16_bf16 v[86:101], v[66:69], v[138:141], v[86:101]
	v_mfma_f32_32x32x16_bf16 v[102:117], v[66:69], v[118:121], v[102:117]
	s_nop 10
	v_cvt_pk_bf16_f32 v78, v86, v87
	v_cvt_pk_bf16_f32 v80, v90, v91
	v_cvt_pk_bf16_f32 v79, v88, v89
	v_cvt_pk_bf16_f32 v81, v92, v93
	ds_read_b128 v[86:89], v212 offset:16384
	ds_read_b128 v[90:93], v212 offset:23552
	v_cvt_pk_bf16_f32 v66, v102, v103
	v_cvt_pk_bf16_f32 v67, v104, v105
	v_cvt_pk_bf16_f32 v68, v106, v107
	v_cvt_pk_bf16_f32 v69, v108, v109
	v_pk_max_i16 v66, v66, 0
	v_pk_max_i16 v67, v67, 0
	v_pk_max_i16 v68, v68, 0
	v_pk_max_i16 v69, v69, 0
	v_pk_max_i16 v78, v78, 0
	v_pk_max_i16 v79, v79, 0
	v_pk_max_i16 v80, v80, 0
	v_pk_max_i16 v81, v81, 0
	v_cvt_pk_bf16_f32 v94, v94, v95
	s_waitcnt lgkmcnt(2)
	v_mfma_f32_32x32x16_bf16 v[18:33], v[74:77], v[78:81], v[18:33]
	v_cvt_pk_bf16_f32 v95, v96, v97
	v_cvt_pk_bf16_f32 v96, v98, v99
	v_cvt_pk_bf16_f32 v97, v100, v101
	v_pk_max_i16 v94, v94, 0
	v_pk_max_i16 v95, v95, 0
	v_pk_max_i16 v96, v96, 0
	v_pk_max_i16 v97, v97, 0
	v_mfma_f32_32x32x16_bf16 v[2:17], v[74:77], v[66:69], v[2:17]
	v_cvt_pk_bf16_f32 v74, v110, v111
	v_cvt_pk_bf16_f32 v75, v112, v113
	v_cvt_pk_bf16_f32 v76, v114, v115
	v_cvt_pk_bf16_f32 v77, v116, v117
	v_pk_max_i16 v74, v74, 0
	v_pk_max_i16 v75, v75, 0
	v_pk_max_i16 v76, v76, 0
	v_pk_max_i16 v77, v77, 0
	s_waitcnt lgkmcnt(0)
	v_mfma_f32_32x32x16_bf16 v[50:65], v[90:93], v[66:69], v[50:65]
	ds_read_b128 v[66:69], v212 offset:24576
	v_mfma_f32_32x32x16_bf16 v[34:49], v[90:93], v[78:81], v[34:49]
	ds_read_b128 v[102:105], v212 offset:7168
	v_mfma_f32_32x32x16_bf16 v[2:17], v[86:89], v[74:77], v[2:17]
	s_waitcnt lgkmcnt(1)
	v_mfma_f32_32x32x16_bf16 v[50:65], v[66:69], v[74:77], v[50:65]
	ds_read_b128 v[74:77], v174 offset:33184
	ds_read_b128 v[78:81], v174 offset:33216
	v_mfma_f32_32x32x16_bf16 v[34:49], v[66:69], v[94:97], v[34:49]
	ds_read_b128 v[66:69], v212 offset:8192
	v_mfma_f32_32x32x16_bf16 v[18:33], v[86:89], v[94:97], v[18:33]
	s_waitcnt lgkmcnt(1)
	v_mfma_f32_32x32x16_bf16 v[86:101], v[102:105], v[126:129], v[70:85]
	v_mfma_f32_32x32x16_bf16 v[70:85], v[102:105], v[134:137], v[70:85]
	ds_read_b128 v[102:105], v212 offset:9216
	v_lshlrev_b32_e32 v135, 2, v1
	v_add_u32_e32 v134, v172, v174
	s_waitcnt lgkmcnt(1)
	v_mfma_f32_32x32x16_bf16 v[86:101], v[66:69], v[122:125], v[86:101]
	v_mfma_f32_32x32x16_bf16 v[70:85], v[66:69], v[146:149], v[70:85]
	ds_read_b128 v[66:69], v212 offset:10240
	s_waitcnt lgkmcnt(1)
	v_mfma_f32_32x32x16_bf16 v[86:101], v[102:105], v[130:133], v[86:101]
	v_mfma_f32_32x32x16_bf16 v[70:85], v[102:105], v[142:145], v[70:85]
	ds_read_b128 v[102:105], v212 offset:17408
	s_waitcnt lgkmcnt(1)
	v_mfma_f32_32x32x16_bf16 v[86:101], v[66:69], v[118:121], v[86:101]
	v_mfma_f32_32x32x16_bf16 v[70:85], v[66:69], v[138:141], v[70:85]
	s_nop 10
	v_cvt_pk_bf16_f32 v68, v90, v91
	v_cvt_pk_bf16_f32 v69, v92, v93
	ds_read_b128 v[90:93], v212 offset:25600
	v_cvt_pk_bf16_f32 v66, v86, v87
	v_cvt_pk_bf16_f32 v67, v88, v89
	v_pk_max_i16 v66, v66, 0
	v_pk_max_i16 v67, v67, 0
	v_pk_max_i16 v68, v68, 0
	v_pk_max_i16 v69, v69, 0
	v_cvt_pk_bf16_f32 v70, v70, v71
	v_cvt_pk_bf16_f32 v71, v72, v73
	s_waitcnt lgkmcnt(1)
	v_mfma_f32_32x32x16_bf16 v[2:17], v[102:105], v[66:69], v[2:17]
	v_cvt_pk_bf16_f32 v72, v74, v75
	v_cvt_pk_bf16_f32 v73, v76, v77
	ds_read_b128 v[74:77], v212 offset:18432
	v_cvt_pk_bf16_f32 v86, v94, v95
	v_cvt_pk_bf16_f32 v87, v96, v97
	v_cvt_pk_bf16_f32 v88, v98, v99
	s_waitcnt lgkmcnt(1)
	v_mfma_f32_32x32x16_bf16 v[50:65], v[90:93], v[66:69], v[50:65]
	ds_read_b128 v[66:69], v212 offset:26624
	v_cvt_pk_bf16_f32 v89, v100, v101
	v_pk_max_i16 v86, v86, 0
	v_pk_max_i16 v87, v87, 0
	v_pk_max_i16 v88, v88, 0
	v_pk_max_i16 v89, v89, 0
	v_pk_max_i16 v70, v70, 0
	v_pk_max_i16 v71, v71, 0
	v_pk_max_i16 v72, v72, 0
	v_pk_max_i16 v73, v73, 0
	v_cvt_pk_bf16_f32 v78, v78, v79
	v_cvt_pk_bf16_f32 v79, v80, v81
	s_waitcnt lgkmcnt(1)
	v_mfma_f32_32x32x16_bf16 v[2:17], v[74:77], v[86:89], v[2:17]
	v_cvt_pk_bf16_f32 v80, v82, v83
	v_cvt_pk_bf16_f32 v81, v84, v85
	v_pk_max_i16 v78, v78, 0
	v_pk_max_i16 v79, v79, 0
	v_pk_max_i16 v80, v80, 0
	v_pk_max_i16 v81, v81, 0
	s_waitcnt lgkmcnt(0)
	v_mfma_f32_32x32x16_bf16 v[50:65], v[66:69], v[86:89], v[50:65]
	v_mfma_f32_32x32x16_bf16 v[34:49], v[90:93], v[70:73], v[34:49]
	s_nop 10
	v_add_f32_e32 v130, v10, v58
	v_add_f32_e32 v131, v11, v59
	v_add_f32_e32 v132, v12, v60
	v_add_f32_e32 v133, v13, v61
	v_add_f32_e32 v138, v4, v52
	v_add_f32_e32 v139, v5, v53
	v_pk_add_f32 v[140:141], v[16:17], v[64:65]
	v_pk_add_f32 v[142:143], v[8:9], v[56:57]
	v_pk_add_f32 v[144:145], v[14:15], v[62:63]
	v_pk_add_f32 v[146:147], v[6:7], v[54:55]
	v_mfma_f32_32x32x16_bf16 v[18:33], v[102:105], v[70:73], v[18:33]
	ds_read2st64_b32 v[70:71], v135 offset0:133 offset1:134
	v_add_f32_e32 v148, v2, v50
	v_add_f32_e32 v149, v3, v51
	v_add_f32_e32 v144, v146, v144
	v_add_f32_e32 v145, v147, v145
	v_pk_add_f32 v[140:141], v[142:143], v[140:141]
	v_pk_add_f32 v[132:133], v[138:139], v[132:133]
	v_pk_add_f32 v[130:131], v[148:149], v[130:131]
	v_pk_add_f32 v[132:133], v[132:133], v[140:141]
	v_pk_add_f32 v[130:131], v[130:131], v[144:145]
	v_mfma_f32_32x32x16_bf16 v[34:49], v[66:69], v[78:81], v[34:49]
	v_pk_mov_b32 v[138:139], v[130:131], v[132:133] op_sel:[1,0]
	v_mov_b32_e32 v131, v133
	s_waitcnt vmcnt(0) lgkmcnt(0)
	v_mul_f32_e32 v66, v175, v70
	v_pk_add_f32 v[130:131], v[138:139], v[130:131]
	ds_write_b32 v173, v66 offset:512
	v_mul_f32_e32 v66, v175, v71
	v_pk_add_f32 v[130:131], v[130:131], v[130:131] op_sel:[0,1] op_sel_hi:[1,0]
	s_waitcnt lgkmcnt(0)
	ds_read_b128 v[102:105], v174 offset:34560
	ds_read_b128 v[98:101], v174 offset:34592
	ds_read_b128 v[110:113], v174 offset:34624
	ds_read_b128 v[106:109], v174 offset:34656
	ds_read_b128 v[114:117], v174 offset:34688
	ds_read_b128 v[122:125], v174 offset:34720
	ds_read_b128 v[118:121], v174 offset:34752
	ds_read_b128 v[126:129], v174 offset:34784
	v_mov_b32_dpp v66, v66 quad_perm:[1,0,3,2] row_mask:0xf bank_mask:0xf bound_ctrl:1
	v_mov_b32_e32 v131, v130
	v_fmac_f32_e32 v66, v175, v71
	s_nop 0
	v_permlane32_swap_b32_e32 v130, v131
	v_add_f32_dpp v66, v66, v66 quad_perm:[2,3,0,1] row_mask:0xf bank_mask:0xf bound_ctrl:1
	v_add_f32_e32 v130, v130, v131
	v_fmamk_f32 v65, v130, 0xbc800000, v65
	v_add_f32_dpp v66, v66, v66 row_half_mirror row_mask:0xf bank_mask:0xf bound_ctrl:1
	v_fmamk_f32 v64, v130, 0xbc800000, v64
	v_fmamk_f32 v63, v130, 0xbc800000, v63
	v_fmamk_f32 v62, v130, 0xbc800000, v62
	v_fmamk_f32 v61, v130, 0xbc800000, v61
	v_fmamk_f32 v60, v130, 0xbc800000, v60
	v_fmamk_f32 v59, v130, 0xbc800000, v59
	v_fmamk_f32 v58, v130, 0xbc800000, v58
	v_fmamk_f32 v57, v130, 0xbc800000, v57
	v_fmamk_f32 v56, v130, 0xbc800000, v56
	v_fmamk_f32 v55, v130, 0xbc800000, v55
	v_fmamk_f32 v54, v130, 0xbc800000, v54
	v_fmamk_f32 v53, v130, 0xbc800000, v53
	v_fmamk_f32 v52, v130, 0xbc800000, v52
	v_fmamk_f32 v51, v130, 0xbc800000, v51
	v_fmac_f32_e32 v50, 0xbc800000, v130
	v_add_f32_dpp v66, v66, v66 row_ror:8 row_mask:0xf bank_mask:0xf bound_ctrl:1
	v_fmamk_f32 v17, v130, 0xbc800000, v17
	v_fmamk_f32 v16, v130, 0xbc800000, v16
	v_fmamk_f32 v15, v130, 0xbc800000, v15
	v_fmamk_f32 v14, v130, 0xbc800000, v14
	v_fmamk_f32 v13, v130, 0xbc800000, v13
	v_fmamk_f32 v12, v130, 0xbc800000, v12
	v_fmamk_f32 v11, v130, 0xbc800000, v11
	v_fmamk_f32 v10, v130, 0xbc800000, v10
	v_fmamk_f32 v9, v130, 0xbc800000, v9
	v_fmamk_f32 v8, v130, 0xbc800000, v8
	v_fmamk_f32 v7, v130, 0xbc800000, v7
	v_fmamk_f32 v6, v130, 0xbc800000, v6
	v_fmamk_f32 v5, v130, 0xbc800000, v5
	v_fmamk_f32 v4, v130, 0xbc800000, v4
	v_fmamk_f32 v3, v130, 0xbc800000, v3
	v_fmac_f32_e32 v2, 0xbc800000, v130
	v_pk_mul_f32 v[130:131], v[54:55], v[54:55]
	v_pk_mul_f32 v[132:133], v[62:63], v[62:63]
	v_pk_mul_f32 v[138:139], v[50:51], v[50:51]
	v_pk_mul_f32 v[140:141], v[58:59], v[58:59]
	v_pk_mul_f32 v[142:143], v[56:57], v[56:57]
	v_pk_mul_f32 v[144:145], v[64:65], v[64:65]
	v_pk_mul_f32 v[146:147], v[52:53], v[52:53]
	v_pk_mul_f32 v[148:149], v[60:61], v[60:61]
	v_mov_b32_e32 v67, v66
	v_pk_fma_f32 v[148:149], v[12:13], v[12:13], v[148:149]
	v_pk_fma_f32 v[146:147], v[4:5], v[4:5], v[146:147]
	v_pk_fma_f32 v[144:145], v[16:17], v[16:17], v[144:145]
	v_pk_fma_f32 v[142:143], v[8:9], v[8:9], v[142:143]
	v_pk_fma_f32 v[140:141], v[10:11], v[10:11], v[140:141]
	v_pk_fma_f32 v[138:139], v[2:3], v[2:3], v[138:139]
	v_pk_fma_f32 v[132:133], v[14:15], v[14:15], v[132:133]
	v_pk_fma_f32 v[130:131], v[6:7], v[6:7], v[130:131]
	v_permlane16_swap_b32_e32 v66, v67
	v_pk_add_f32 v[130:131], v[130:131], v[132:133]
	v_pk_add_f32 v[132:133], v[138:139], v[140:141]
	v_pk_add_f32 v[138:139], v[142:143], v[144:145]
	v_pk_add_f32 v[140:141], v[146:147], v[148:149]
	v_mfma_f32_32x32x16_bf16 v[18:33], v[74:77], v[78:81], v[18:33]
	v_add_f32_e32 v136, v66, v67
	ds_read_b128 v[70:73], v134 offset:512
	ds_read_b128 v[66:69], v134 offset:544
	ds_read_b128 v[78:81], v134 offset:576
	ds_read_b128 v[74:77], v134 offset:608
	ds_read_b128 v[82:85], v134 offset:640
	ds_read_b128 v[90:93], v134 offset:672
	ds_read_b128 v[86:89], v134 offset:704
	ds_read_b128 v[94:97], v134 offset:736
	v_pk_add_f32 v[138:139], v[140:141], v[138:139]
	v_pk_add_f32 v[130:131], v[132:133], v[130:131]
	s_waitcnt lgkmcnt(8)
	v_pk_mul_f32 v[140:141], v[126:127], v[62:63]
	v_pk_mov_b32 v[132:133], v[130:131], v[138:139] op_sel:[1,0]
	v_mov_b32_e32 v131, v139
	v_pk_mul_f32 v[138:139], v[122:123], v[54:55]
	v_pk_mul_f32 v[142:143], v[114:115], v[50:51]
	v_pk_mul_f32 v[144:145], v[118:119], v[58:59]
	v_pk_mul_f32 v[146:147], v[124:125], v[56:57]
	v_pk_mul_f32 v[148:149], v[128:129], v[64:65]
	v_pk_mul_f32 v[154:155], v[116:117], v[52:53]
	v_pk_mul_f32 v[156:157], v[120:121], v[60:61]
	v_pk_fma_f32 v[154:155], v[104:105], v[4:5], v[154:155]
	v_pk_fma_f32 v[156:157], v[112:113], v[12:13], v[156:157]
	v_pk_fma_f32 v[148:149], v[108:109], v[16:17], v[148:149]
	v_pk_fma_f32 v[146:147], v[100:101], v[8:9], v[146:147]
	v_pk_fma_f32 v[144:145], v[110:111], v[10:11], v[144:145]
	v_pk_fma_f32 v[142:143], v[102:103], v[2:3], v[142:143]
	v_pk_fma_f32 v[140:141], v[106:107], v[14:15], v[140:141]
	v_pk_fma_f32 v[138:139], v[98:99], v[6:7], v[138:139]
	v_pk_add_f32 v[130:131], v[132:133], v[130:131]
	v_pk_add_f32 v[138:139], v[138:139], v[140:141]
	v_pk_add_f32 v[140:141], v[142:143], v[144:145]
	v_pk_add_f32 v[142:143], v[146:147], v[148:149]
	v_pk_add_f32 v[144:145], v[154:155], v[156:157]
	v_pk_add_f32 v[132:133], v[130:131], v[130:131] op_sel:[0,1] op_sel_hi:[1,0]
	v_pk_add_f32 v[142:143], v[144:145], v[142:143]
	v_pk_add_f32 v[138:139], v[140:141], v[138:139]
	v_add_f32_e32 v133, v142, v143
	v_add_f32_e32 v130, v138, v139
	s_waitcnt lgkmcnt(2)
	v_pk_mul_f32 v[138:139], v[90:91], v[54:55]
	s_waitcnt lgkmcnt(0)
	v_pk_mul_f32 v[140:141], v[94:95], v[62:63]
	v_pk_mul_f32 v[142:143], v[82:83], v[50:51]
	v_pk_mul_f32 v[144:145], v[86:87], v[58:59]
	v_pk_mul_f32 v[146:147], v[92:93], v[56:57]
	v_pk_mul_f32 v[148:149], v[96:97], v[64:65]
	v_pk_mul_f32 v[154:155], v[84:85], v[52:53]
	v_pk_mul_f32 v[156:157], v[88:89], v[60:61]
	v_add_f32_e32 v130, v130, v133
	v_pk_fma_f32 v[156:157], v[80:81], v[12:13], v[156:157]
	v_pk_fma_f32 v[154:155], v[72:73], v[4:5], v[154:155]
	v_pk_fma_f32 v[148:149], v[76:77], v[16:17], v[148:149]
	v_pk_fma_f32 v[146:147], v[68:69], v[8:9], v[146:147]
	v_pk_fma_f32 v[144:145], v[78:79], v[10:11], v[144:145]
	v_pk_fma_f32 v[142:143], v[70:71], v[2:3], v[142:143]
	v_pk_fma_f32 v[140:141], v[74:75], v[14:15], v[140:141]
	v_pk_fma_f32 v[138:139], v[66:67], v[6:7], v[138:139]
	v_mov_b32_e32 v133, v130
	v_pk_add_f32 v[138:139], v[138:139], v[140:141]
	v_pk_add_f32 v[140:141], v[142:143], v[144:145]
	v_pk_add_f32 v[142:143], v[146:147], v[148:149]
	v_pk_add_f32 v[144:145], v[154:155], v[156:157]
	v_permlane32_swap_b32_e32 v130, v133
	v_pk_add_f32 v[142:143], v[144:145], v[142:143]
	v_add_f32_e32 v160, v130, v133
	v_pk_add_f32 v[138:139], v[140:141], v[138:139]
	v_add_f32_e32 v133, v142, v143
	v_pk_add_f32 v[140:141], v[26:27], v[42:43]
	v_pk_add_f32 v[142:143], v[28:29], v[44:45]
	v_pk_add_f32 v[144:145], v[20:21], v[36:37]
	v_pk_add_f32 v[146:147], v[32:33], v[48:49]
	v_pk_add_f32 v[148:149], v[24:25], v[40:41]
	v_pk_add_f32 v[154:155], v[30:31], v[46:47]
	v_pk_add_f32 v[156:157], v[22:23], v[38:39]
	v_pk_add_f32 v[158:159], v[18:19], v[34:35]
	v_pk_add_f32 v[154:155], v[156:157], v[154:155]
	v_pk_add_f32 v[146:147], v[148:149], v[146:147]
	v_pk_add_f32 v[142:143], v[144:145], v[142:143]
	v_pk_add_f32 v[140:141], v[158:159], v[140:141]
	v_pk_add_f32 v[142:143], v[142:143], v[146:147]
	v_pk_add_f32 v[140:141], v[140:141], v[154:155]
	v_add_f32_e32 v130, v138, v139
	v_pk_mov_b32 v[144:145], v[140:141], v[142:143] op_sel:[1,0]
	v_mov_b32_e32 v141, v143
	v_pk_add_f32 v[140:141], v[144:145], v[140:141]
	v_add_f32_e32 v133, v130, v133
	v_pk_add_f32 v[140:141], v[140:141], v[140:141] op_sel:[0,1] op_sel_hi:[1,0]
	v_mov_b32_e32 v131, v132
	v_mov_b32_e32 v130, v140
	s_nop 1
	v_permlane32_swap_b32_e32 v140, v130
	v_add_f32_e32 v130, v140, v130
	v_fmamk_f32 v49, v130, 0xbc800000, v49
	v_fmamk_f32 v48, v130, 0xbc800000, v48
	v_fmamk_f32 v47, v130, 0xbc800000, v47
	v_fmamk_f32 v46, v130, 0xbc800000, v46
	v_fmamk_f32 v45, v130, 0xbc800000, v45
	v_fmamk_f32 v44, v130, 0xbc800000, v44
	v_fmamk_f32 v43, v130, 0xbc800000, v43
	v_fmamk_f32 v42, v130, 0xbc800000, v42
	v_fmamk_f32 v41, v130, 0xbc800000, v41
	v_fmamk_f32 v40, v130, 0xbc800000, v40
	v_fmamk_f32 v39, v130, 0xbc800000, v39
	v_fmamk_f32 v38, v130, 0xbc800000, v38
	v_fmamk_f32 v37, v130, 0xbc800000, v37
	v_fmamk_f32 v36, v130, 0xbc800000, v36
	v_fmamk_f32 v35, v130, 0xbc800000, v35
	v_fmac_f32_e32 v34, 0xbc800000, v130
	v_fmamk_f32 v33, v130, 0xbc800000, v33
	v_fmamk_f32 v32, v130, 0xbc800000, v32
	v_fmamk_f32 v31, v130, 0xbc800000, v31
	v_fmamk_f32 v30, v130, 0xbc800000, v30
	v_fmamk_f32 v29, v130, 0xbc800000, v29
	v_fmamk_f32 v28, v130, 0xbc800000, v28
	v_fmamk_f32 v27, v130, 0xbc800000, v27
	v_fmamk_f32 v26, v130, 0xbc800000, v26
	v_fmamk_f32 v25, v130, 0xbc800000, v25
	v_fmamk_f32 v24, v130, 0xbc800000, v24
	v_fmamk_f32 v23, v130, 0xbc800000, v23
	v_fmamk_f32 v22, v130, 0xbc800000, v22
	v_fmamk_f32 v21, v130, 0xbc800000, v21
	v_fmamk_f32 v20, v130, 0xbc800000, v20
	v_fmamk_f32 v19, v130, 0xbc800000, v19
	v_fmac_f32_e32 v18, 0xbc800000, v130
	v_pk_mul_f32 v[140:141], v[38:39], v[38:39]
	v_pk_mul_f32 v[142:143], v[46:47], v[46:47]
	v_pk_mul_f32 v[144:145], v[34:35], v[34:35]
	v_pk_mul_f32 v[146:147], v[42:43], v[42:43]
	v_pk_mul_f32 v[148:149], v[40:41], v[40:41]
	v_pk_mul_f32 v[154:155], v[48:49], v[48:49]
	v_pk_mul_f32 v[156:157], v[36:37], v[36:37]
	v_pk_mul_f32 v[158:159], v[44:45], v[44:45]
	v_pk_fma_f32 v[156:157], v[20:21], v[20:21], v[156:157]
	v_pk_fma_f32 v[158:159], v[28:29], v[28:29], v[158:159]
	v_pk_fma_f32 v[154:155], v[32:33], v[32:33], v[154:155]
	v_pk_fma_f32 v[148:149], v[24:25], v[24:25], v[148:149]
	v_pk_fma_f32 v[146:147], v[26:27], v[26:27], v[146:147]
	v_pk_fma_f32 v[144:145], v[18:19], v[18:19], v[144:145]
	v_pk_fma_f32 v[142:143], v[30:31], v[30:31], v[142:143]
	v_pk_fma_f32 v[140:141], v[22:23], v[22:23], v[140:141]
	v_permlane32_swap_b32_e32 v132, v131
	v_pk_add_f32 v[140:141], v[140:141], v[142:143]
	v_pk_add_f32 v[142:143], v[144:145], v[146:147]
	v_pk_add_f32 v[144:145], v[148:149], v[154:155]
	v_pk_add_f32 v[146:147], v[156:157], v[158:159]
	v_pk_add_f32 v[140:141], v[142:143], v[140:141]
	v_pk_add_f32 v[144:145], v[146:147], v[144:145]
	v_pk_mul_f32 v[122:123], v[122:123], v[38:39]
	v_pk_mov_b32 v[142:143], v[140:141], v[144:145] op_sel:[1,0]
	v_mov_b32_e32 v141, v145
	v_pk_add_f32 v[140:141], v[142:143], v[140:141]
	v_pk_mul_f32 v[126:127], v[126:127], v[46:47]
	v_pk_add_f32 v[140:141], v[140:141], v[140:141] op_sel:[0,1] op_sel_hi:[1,0]
	v_pk_mul_f32 v[114:115], v[114:115], v[34:35]
	v_mov_b32_e32 v130, v140
	s_nop 1
	v_permlane32_swap_b32_e32 v140, v130
	v_mov_b32_e32 v141, v132
	v_pk_add_f32 v[130:131], v[140:141], v[130:131]
	v_pk_mul_f32 v[118:119], v[118:119], v[42:43]
	v_pk_fma_f32 v[130:131], v[130:131], s[0:1], v[152:153] op_sel_hi:[1,0,0]
	v_pk_mul_f32 v[124:125], v[124:125], v[40:41]
	v_mul_f32_e32 v132, 0x4b800000, v131
	v_cmp_gt_f32_e32 vcc, s1, v131
	v_pk_mul_f32 v[128:129], v[128:129], v[48:49]
	v_pk_mul_f32 v[116:117], v[116:117], v[36:37]
	v_pk_mul_f32 v[120:121], v[120:121], v[44:45]
	v_cndmask_b32_e32 v131, v131, v132, vcc
	v_mul_f32_e32 v132, 0x4b800000, v130
	v_cmp_gt_f32_e64 s[0:1], s1, v130
	v_pk_fma_f32 v[112:113], v[112:113], v[28:29], v[120:121]
	v_pk_fma_f32 v[104:105], v[104:105], v[20:21], v[116:117]
	v_pk_fma_f32 v[108:109], v[108:109], v[32:33], v[128:129]
	v_pk_fma_f32 v[100:101], v[100:101], v[24:25], v[124:125]
	v_pk_fma_f32 v[110:111], v[110:111], v[26:27], v[118:119]
	v_pk_fma_f32 v[102:103], v[102:103], v[18:19], v[114:115]
	v_pk_fma_f32 v[106:107], v[106:107], v[30:31], v[126:127]
	v_pk_fma_f32 v[98:99], v[98:99], v[22:23], v[122:123]
	v_rsq_f32_e32 v131, v131
	v_cndmask_b32_e64 v130, v130, v132, s[0:1]
	v_pk_add_f32 v[98:99], v[98:99], v[106:107]
	v_pk_add_f32 v[102:103], v[102:103], v[110:111]
	v_pk_add_f32 v[100:101], v[100:101], v[108:109]
	v_pk_add_f32 v[104:105], v[104:105], v[112:113]
	v_rsq_f32_e32 v132, v130
	v_pk_add_f32 v[100:101], v[104:105], v[100:101]
	v_pk_add_f32 v[98:99], v[102:103], v[98:99]
	v_mul_f32_e32 v130, 0x45800000, v131
	v_add_f32_e32 v98, v98, v99
	v_add_f32_e32 v99, v100, v101
	v_add_f32_e32 v98, v98, v99
	v_mov_b32_e32 v99, v98
	v_pk_mul_f32 v[90:91], v[90:91], v[38:39]
	v_pk_mul_f32 v[94:95], v[94:95], v[46:47]
	v_pk_mul_f32 v[82:83], v[82:83], v[34:35]
	v_pk_mul_f32 v[86:87], v[86:87], v[42:43]
	v_cndmask_b32_e32 v130, v131, v130, vcc
	v_mul_f32_e32 v131, 0x45800000, v132
	v_permlane32_swap_b32_e32 v98, v99
	v_pk_fma_f32 v[78:79], v[78:79], v[26:27], v[86:87]
	v_pk_fma_f32 v[70:71], v[70:71], v[18:19], v[82:83]
	v_pk_fma_f32 v[74:75], v[74:75], v[30:31], v[94:95]
	v_pk_fma_f32 v[66:67], v[66:67], v[22:23], v[90:91]
	v_cndmask_b32_e64 v131, v132, v131, s[0:1]
	v_add_f32_e32 v98, v98, v99
	v_pk_add_f32 v[66:67], v[66:67], v[74:75]
	v_pk_add_f32 v[70:71], v[70:71], v[78:79]
	v_mul_f32_e32 v139, v160, v130
	v_mul_f32_e32 v98, v98, v131
	v_pk_add_f32 v[66:67], v[70:71], v[66:67]
	v_cmp_gt_u32_e32 vcc, 32, v1
	v_add_f32_e32 v66, v66, v67
	v_pk_mul_f32 v[92:93], v[92:93], v[40:41]
	v_cndmask_b32_e32 v67, v98, v139, vcc
	v_add_f32_e32 v67, s12, v67
	v_pk_mul_f32 v[96:97], v[96:97], v[48:49]
	v_pk_mul_f32 v[84:85], v[84:85], v[36:37]
	v_pk_mul_f32 v[88:89], v[88:89], v[44:45]
	v_mul_f32_e32 v67, 0xbfb8aa3b, v67
	v_pk_fma_f32 v[80:81], v[80:81], v[28:29], v[88:89]
	v_pk_fma_f32 v[72:73], v[72:73], v[20:21], v[84:85]
	v_pk_fma_f32 v[76:77], v[76:77], v[32:33], v[96:97]
	v_pk_fma_f32 v[68:69], v[68:69], v[24:25], v[92:93]
	v_exp_f32_e32 v70, v67
	v_pk_add_f32 v[68:69], v[68:69], v[76:77]
	v_pk_add_f32 v[72:73], v[72:73], v[80:81]
	v_cmp_lt_i32_e64 s[0:1], 0, v151
	v_pk_add_f32 v[68:69], v[72:73], v[68:69]
	v_mov_b32_e32 v137, v136
	v_add_f32_e32 v67, v68, v69
	v_add_f32_e32 v67, v66, v67
	v_add_f32_e32 v66, 1.0, v70
	v_rcp_f32_e32 v66, v66
	v_mov_b32_e32 v69, 0xff800000
	v_mov_b32_e32 v138, v133
	v_mov_b32_e32 v68, v67
	v_cndmask_b32_e64 v70, v69, v66, s[0:1]
	v_mbcnt_lo_u32_b32 v66, -1, 0
	v_mbcnt_hi_u32_b32 v66, -1, v66
	v_permlane32_swap_b32_e32 v136, v137
	v_permlane32_swap_b32_e32 v133, v138
	v_permlane32_swap_b32_e32 v67, v68
	v_and_b32_e32 v86, 64, v66
	s_mov_b32 s14, 8
	s_mov_b32 s13, 0
	v_mov_b32_e32 v66, 0
	s_waitcnt lgkmcnt(0)
